# one static s_setprio 1 for waves 4-7 at kernel entry, all per-segment s_setprio removed (on top of v59)
# speedup vs baseline: 1.0070x; 1.0050x over previous
_Z3fwd4Args:
	s_mov_b32 s96, s2
	s_load_dwordx4 s[44:47], s[0:1], 0xc8
	s_add_u32 s2, s0, 0xd8
	s_addc_u32 s3, s1, 0
	v_readfirstlane_b32 s10, v0
	v_writelane_b32 v252, s2, 0
	s_nop 1
	v_writelane_b32 v252, s3, 1
	s_movk_i32 s2, 0x200
	v_cmp_gt_u32_e32 vcc, s2, v0
	s_and_saveexec_b64 s[4:5], vcc
	v_lshl_add_u32 v1, v0, 2, 0
	v_add_u32_e32 v1, 0x24c00, v1
	v_mov_b32_e32 v2, 0
	ds_write_b32 v1, v2
	s_or_b64 exec, exec, s[4:5]
	s_lshr_b32 s4, s10, 6
	s_cmp_ge_u32 s4, 4
	s_cbranch_scc0 .Lprio_static_done
	s_setprio 1
.Lprio_static_done:
	s_load_dword s91, s[0:1], 0xd8
	s_waitcnt lgkmcnt(0)
	s_add_u32 s2, s44, 0x4000
	s_addc_u32 s3, s45, 0
	v_writelane_b32 v252, s2, 2
	s_barrier
	s_nop 0
	v_writelane_b32 v252, s3, 3
	s_getreg_b32 s2, hwreg(HW_REG_XCC_ID, 0, 4)
	s_and_b32 s2, s2, 15
	v_writelane_b32 v252, s2, 4
	v_cmp_eq_u32_e64 s[2:3], 0, v0
	s_mov_b64 s[6:7], exec
	s_nop 0
	v_writelane_b32 v252, s2, 5
	s_nop 1
	v_writelane_b32 v252, s3, 6
	s_and_b64 s[2:3], s[6:7], s[2:3]
	s_mov_b64 exec, s[2:3]
	s_cbranch_execz .LBB0_5
	s_mov_b64 s[8:9], exec
	v_mbcnt_lo_u32_b32 v1, s8, 0
	v_mbcnt_hi_u32_b32 v1, s9, v1
	v_cmp_eq_u32_e32 vcc, 0, v1
	s_and_b64 s[2:3], exec, vcc
	s_mov_b64 exec, s[2:3]
	s_cbranch_execz .LBB0_5
	v_readlane_b32 s2, v252, 4
	s_lshl_b32 s2, s2, 8
	s_bcnt1_i32_b64 s3, s[8:9]
	v_mov_b32_e32 v1, s2
	v_mov_b32_e32 v2, s3
	v_readlane_b32 s2, v252, 2
	v_readlane_b32 s3, v252, 3
	s_nop 4
	global_atomic_add v1, v2, s[2:3] offset:1024

.Lmoe_ix_ready_0:
.LBB0_1005:
	ds_read_b128 v[152:155], v158
	ds_read_b128 v[166:169], v158 offset:1024
	ds_read_b128 v[170:173], v158 offset:2048
	ds_read_b128 v[174:177], v158 offset:3072
	ds_read_b128 v[178:181], v159
	ds_read_b128 v[182:185], v159 offset:1024
	ds_read_b128 v[186:189], v159 offset:2048
	ds_read_b128 v[190:193], v159 offset:3072
	s_add_u32 s40, s64, s10
	s_addc_u32 s41, s65, s11
	s_add_u32 s38, s10, 0x100
	s_addc_u32 s39, s11, 0
	s_cmpk_eq_i32 s10, 0xf00
	s_cselect_b64 vcc, -1, 0
	s_and_b64 s[2:3], vcc, exec
	s_cselect_b32 s41, s31, s41
	s_cselect_b32 s40, s37, s40
	s_cselect_b32 s67, 0, s38
	v_lshl_add_u64 v[226:227], v[146:147], 0, s[10:11]
	s_add_i32 m0, s49, 0xc000
	ds_read_b128 v[194:197], v160
	ds_read_b128 v[198:201], v160 offset:1024
	ds_read_b128 v[202:205], v160 offset:2048
	ds_read_b128 v[206:209], v160 offset:3072
	ds_read_b128 v[210:213], v160 offset:4096
	ds_read_b128 v[214:217], v160 offset:5120
	ds_read_b128 v[218:221], v160 offset:6144
	ds_read_b128 v[222:225], v160 offset:7168
	global_load_lds_dwordx4 v[226:227], off
	v_lshl_add_u64 v[226:227], v[144:145], 0, s[10:11]
	s_add_i32 m0, s49, 0xe000
	s_nop 0
	global_load_lds_dwordx4 v[226:227], off
	s_waitcnt vmcnt(8)
	s_waitcnt lgkmcnt(0)
	s_barrier
	s_waitcnt lgkmcnt(0)
	v_mfma_f32_16x16x32_bf16 v[126:129], v[152:155], v[194:197], v[126:129]
	v_mfma_f32_16x16x32_bf16 v[122:125], v[170:173], v[194:197], v[122:125]
	v_mfma_f32_16x16x32_bf16 v[110:113], v[152:155], v[202:205], v[110:113]
	v_mfma_f32_16x16x32_bf16 v[106:109], v[170:173], v[202:205], v[106:109]
	v_mfma_f32_16x16x32_bf16 v[94:97], v[152:155], v[210:213], v[94:97]
	v_mfma_f32_16x16x32_bf16 v[90:93], v[170:173], v[210:213], v[90:93]
	v_mfma_f32_16x16x32_bf16 v[78:81], v[152:155], v[218:221], v[78:81]
	v_mfma_f32_16x16x32_bf16 v[74:77], v[170:173], v[218:221], v[74:77]
	v_mfma_f32_16x16x32_bf16 v[126:129], v[166:169], v[198:201], v[126:129]
	v_mfma_f32_16x16x32_bf16 v[122:125], v[174:177], v[198:201], v[122:125]
	v_mfma_f32_16x16x32_bf16 v[110:113], v[166:169], v[206:209], v[110:113]
	v_mfma_f32_16x16x32_bf16 v[106:109], v[174:177], v[206:209], v[106:109]
	v_mfma_f32_16x16x32_bf16 v[94:97], v[166:169], v[214:217], v[94:97]
	v_mfma_f32_16x16x32_bf16 v[90:93], v[174:177], v[214:217], v[90:93]
	v_mfma_f32_16x16x32_bf16 v[78:81], v[166:169], v[222:225], v[78:81]
	v_mfma_f32_16x16x32_bf16 v[74:77], v[174:177], v[222:225], v[74:77]
	v_mfma_f32_16x16x32_bf16 v[118:121], v[178:181], v[194:197], v[118:121]
	v_mfma_f32_16x16x32_bf16 v[114:117], v[186:189], v[194:197], v[114:117]
	v_mfma_f32_16x16x32_bf16 v[102:105], v[178:181], v[202:205], v[102:105]
	v_mfma_f32_16x16x32_bf16 v[98:101], v[186:189], v[202:205], v[98:101]
	v_mfma_f32_16x16x32_bf16 v[86:89], v[178:181], v[210:213], v[86:89]
	v_mfma_f32_16x16x32_bf16 v[82:85], v[186:189], v[210:213], v[82:85]
	v_mfma_f32_16x16x32_bf16 v[70:73], v[178:181], v[218:221], v[70:73]
	v_mfma_f32_16x16x32_bf16 v[66:69], v[186:189], v[218:221], v[66:69]
	v_mfma_f32_16x16x32_bf16 v[118:121], v[182:185], v[198:201], v[118:121]
	v_mfma_f32_16x16x32_bf16 v[114:117], v[190:193], v[198:201], v[114:117]
	v_mfma_f32_16x16x32_bf16 v[102:105], v[182:185], v[206:209], v[102:105]
	v_mfma_f32_16x16x32_bf16 v[98:101], v[190:193], v[206:209], v[98:101]
	v_mfma_f32_16x16x32_bf16 v[86:89], v[182:185], v[214:217], v[86:89]
	v_mfma_f32_16x16x32_bf16 v[82:85], v[190:193], v[214:217], v[82:85]
	v_mfma_f32_16x16x32_bf16 v[70:73], v[182:185], v[222:225], v[70:73]
	v_mfma_f32_16x16x32_bf16 v[66:69], v[190:193], v[222:225], v[66:69]
	s_barrier
	s_add_i32 s2, s61, s48
	v_lshl_add_u64 v[226:227], s[40:41], 0, v[132:133]
	s_mov_b32 m0, s2
	ds_read_b128 v[194:197], v160 offset:16384
	ds_read_b128 v[198:201], v160 offset:17408
	ds_read_b128 v[202:205], v160 offset:18432
	ds_read_b128 v[206:209], v160 offset:19456
	ds_read_b128 v[210:213], v160 offset:20480
	ds_read_b128 v[214:217], v160 offset:21504
	ds_read_b128 v[218:221], v160 offset:22528
	ds_read_b128 v[222:225], v160 offset:23552
	global_load_lds_dwordx4 v[226:227], off
	s_add_i32 m0, s2, 0x2000
	s_add_u32 s2, s40, 0x80000
	v_lshl_add_u64 v[228:229], s[40:41], 0, v[134:135]
	s_addc_u32 s3, s41, 0
	s_add_i32 s10, s62, s48
	global_load_lds_dwordx4 v[228:229], off
	v_lshl_add_u64 v[230:231], s[2:3], 0, v[132:133]
	s_mov_b32 m0, s10
	v_cndmask_b32_e32 v130, v148, v164, vcc
	global_load_lds_dwordx4 v[230:231], off
	s_add_i32 m0, s10, 0x2000
	v_lshl_add_u64 v[230:231], s[2:3], 0, v[134:135]
	s_add_u32 s2, s16, s67
	global_load_lds_dwordx4 v[230:231], off
	s_addc_u32 s3, s17, 0
	s_mov_b32 m0, s49
	v_lshl_add_u64 v[230:231], s[2:3], 0, v[130:131]
	global_load_lds_dwordx4 v130, s[2:3]
	v_cndmask_b32_e32 v130, v140, v163, vcc
	s_mov_b32 m0, s50
	v_lshl_add_u64 v[232:233], s[2:3], 0, v[130:131]
	global_load_lds_dwordx4 v130, s[2:3]
	s_waitcnt vmcnt(8)
	s_waitcnt lgkmcnt(0)
	s_barrier
	s_waitcnt lgkmcnt(0)
	v_mfma_f32_16x16x32_bf16 v[62:65], v[152:155], v[194:197], v[62:65]
	v_mfma_f32_16x16x32_bf16 v[58:61], v[170:173], v[194:197], v[58:61]
	v_mfma_f32_16x16x32_bf16 v[46:49], v[152:155], v[202:205], v[46:49]
	v_mfma_f32_16x16x32_bf16 v[42:45], v[170:173], v[202:205], v[42:45]
	v_mfma_f32_16x16x32_bf16 v[30:33], v[152:155], v[210:213], v[30:33]
	v_mfma_f32_16x16x32_bf16 v[26:29], v[170:173], v[210:213], v[26:29]
	v_mfma_f32_16x16x32_bf16 v[14:17], v[152:155], v[218:221], v[14:17]
	v_mfma_f32_16x16x32_bf16 v[10:13], v[170:173], v[218:221], v[10:13]
	v_mfma_f32_16x16x32_bf16 v[62:65], v[166:169], v[198:201], v[62:65]
	v_mfma_f32_16x16x32_bf16 v[58:61], v[174:177], v[198:201], v[58:61]
	v_mfma_f32_16x16x32_bf16 v[46:49], v[166:169], v[206:209], v[46:49]
	v_mfma_f32_16x16x32_bf16 v[42:45], v[174:177], v[206:209], v[42:45]
	v_mfma_f32_16x16x32_bf16 v[30:33], v[166:169], v[214:217], v[30:33]
	v_mfma_f32_16x16x32_bf16 v[26:29], v[174:177], v[214:217], v[26:29]
	v_mfma_f32_16x16x32_bf16 v[14:17], v[166:169], v[222:225], v[14:17]
	v_mfma_f32_16x16x32_bf16 v[10:13], v[174:177], v[222:225], v[10:13]
	v_mfma_f32_16x16x32_bf16 v[54:57], v[178:181], v[194:197], v[54:57]
	v_mfma_f32_16x16x32_bf16 v[50:53], v[186:189], v[194:197], v[50:53]
	v_mfma_f32_16x16x32_bf16 v[38:41], v[178:181], v[202:205], v[38:41]
	v_mfma_f32_16x16x32_bf16 v[34:37], v[186:189], v[202:205], v[34:37]
	v_mfma_f32_16x16x32_bf16 v[22:25], v[178:181], v[210:213], v[22:25]
	v_mfma_f32_16x16x32_bf16 v[18:21], v[186:189], v[210:213], v[18:21]
	v_mfma_f32_16x16x32_bf16 v[6:9], v[178:181], v[218:221], v[6:9]
	v_mfma_f32_16x16x32_bf16 v[2:5], v[186:189], v[218:221], v[2:5]
	v_mfma_f32_16x16x32_bf16 v[54:57], v[182:185], v[198:201], v[54:57]
	v_mfma_f32_16x16x32_bf16 v[50:53], v[190:193], v[198:201], v[50:53]
	v_mfma_f32_16x16x32_bf16 v[38:41], v[182:185], v[206:209], v[38:41]
	v_mfma_f32_16x16x32_bf16 v[34:37], v[190:193], v[206:209], v[34:37]
	v_mfma_f32_16x16x32_bf16 v[22:25], v[182:185], v[214:217], v[22:25]
	v_mfma_f32_16x16x32_bf16 v[18:21], v[190:193], v[214:217], v[18:21]
	v_mfma_f32_16x16x32_bf16 v[6:9], v[182:185], v[222:225], v[6:9]
	v_mfma_f32_16x16x32_bf16 v[2:5], v[190:193], v[222:225], v[2:5]
	s_barrier
	s_add_i32 s10, 0, 0x18000
	v_add_u32_e32 v130, s10, v156
	s_add_i32 s11, 0, 0x1c000
	ds_read_b128 v[152:155], v130
	ds_read_b128 v[166:169], v130 offset:1024
	ds_read_b128 v[170:173], v130 offset:2048
	ds_read_b128 v[174:177], v130 offset:3072
	v_add_u32_e32 v130, s11, v156
	ds_read_b128 v[178:181], v130
	ds_read_b128 v[182:185], v130 offset:1024
	ds_read_b128 v[186:189], v130 offset:2048
	ds_read_b128 v[190:193], v130 offset:3072
	s_mov_b32 m0, s51
	v_cndmask_b32_e32 v130, v138, v161, vcc
	ds_read_b128 v[194:197], v160 offset:32768
	ds_read_b128 v[198:201], v160 offset:33792
	ds_read_b128 v[202:205], v160 offset:34816
	ds_read_b128 v[206:209], v160 offset:35840
	ds_read_b128 v[210:213], v160 offset:36864
	ds_read_b128 v[214:217], v160 offset:37888
	ds_read_b128 v[218:221], v160 offset:38912
	ds_read_b128 v[222:225], v160 offset:39936
	global_load_lds_dwordx4 v130, s[2:3]
	v_cndmask_b32_e32 v130, v142, v162, vcc
	s_mov_b32 m0, s52
	s_nop 0
	global_load_lds_dwordx4 v130, s[2:3]
	s_waitcnt vmcnt(8)
	s_waitcnt lgkmcnt(0)
	s_barrier
	s_waitcnt lgkmcnt(0)
	v_mfma_f32_16x16x32_bf16 v[126:129], v[152:155], v[194:197], v[126:129]
	v_mfma_f32_16x16x32_bf16 v[122:125], v[170:173], v[194:197], v[122:125]
	v_mfma_f32_16x16x32_bf16 v[110:113], v[152:155], v[202:205], v[110:113]
	v_mfma_f32_16x16x32_bf16 v[106:109], v[170:173], v[202:205], v[106:109]
	v_mfma_f32_16x16x32_bf16 v[94:97], v[152:155], v[210:213], v[94:97]
	v_mfma_f32_16x16x32_bf16 v[90:93], v[170:173], v[210:213], v[90:93]
	v_mfma_f32_16x16x32_bf16 v[78:81], v[152:155], v[218:221], v[78:81]
	v_mfma_f32_16x16x32_bf16 v[74:77], v[170:173], v[218:221], v[74:77]
	v_mfma_f32_16x16x32_bf16 v[126:129], v[166:169], v[198:201], v[126:129]
	v_mfma_f32_16x16x32_bf16 v[122:125], v[174:177], v[198:201], v[122:125]
	v_mfma_f32_16x16x32_bf16 v[110:113], v[166:169], v[206:209], v[110:113]
	v_mfma_f32_16x16x32_bf16 v[106:109], v[174:177], v[206:209], v[106:109]
	v_mfma_f32_16x16x32_bf16 v[94:97], v[166:169], v[214:217], v[94:97]
	v_mfma_f32_16x16x32_bf16 v[90:93], v[174:177], v[214:217], v[90:93]
	v_mfma_f32_16x16x32_bf16 v[78:81], v[166:169], v[222:225], v[78:81]
	v_mfma_f32_16x16x32_bf16 v[74:77], v[174:177], v[222:225], v[74:77]
	v_mfma_f32_16x16x32_bf16 v[118:121], v[178:181], v[194:197], v[118:121]
	v_mfma_f32_16x16x32_bf16 v[114:117], v[186:189], v[194:197], v[114:117]
	v_mfma_f32_16x16x32_bf16 v[102:105], v[178:181], v[202:205], v[102:105]
	v_mfma_f32_16x16x32_bf16 v[98:101], v[186:189], v[202:205], v[98:101]
	v_mfma_f32_16x16x32_bf16 v[86:89], v[178:181], v[210:213], v[86:89]
	v_mfma_f32_16x16x32_bf16 v[82:85], v[186:189], v[210:213], v[82:85]
	v_mfma_f32_16x16x32_bf16 v[70:73], v[178:181], v[218:221], v[70:73]
	v_mfma_f32_16x16x32_bf16 v[66:69], v[186:189], v[218:221], v[66:69]
	v_mfma_f32_16x16x32_bf16 v[118:121], v[182:185], v[198:201], v[118:121]
	v_mfma_f32_16x16x32_bf16 v[114:117], v[190:193], v[198:201], v[114:117]
	v_mfma_f32_16x16x32_bf16 v[102:105], v[182:185], v[206:209], v[102:105]
	v_mfma_f32_16x16x32_bf16 v[98:101], v[190:193], v[206:209], v[98:101]
	v_mfma_f32_16x16x32_bf16 v[86:89], v[182:185], v[214:217], v[86:89]
	v_mfma_f32_16x16x32_bf16 v[82:85], v[190:193], v[214:217], v[82:85]
	v_mfma_f32_16x16x32_bf16 v[70:73], v[182:185], v[222:225], v[70:73]
	v_mfma_f32_16x16x32_bf16 v[66:69], v[190:193], v[222:225], v[66:69]
	s_barrier
	s_add_i32 s2, s10, s48
	v_lshl_add_u64 v[226:227], v[226:227], 0, s[20:21]
	s_mov_b32 m0, s2
	ds_read_b128 v[194:197], v160 offset:49152
	ds_read_b128 v[198:201], v160 offset:50176
	ds_read_b128 v[202:205], v160 offset:51200
	ds_read_b128 v[206:209], v160 offset:52224
	ds_read_b128 v[210:213], v160 offset:53248
	ds_read_b128 v[214:217], v160 offset:54272
	ds_read_b128 v[218:221], v160 offset:55296
	ds_read_b128 v[222:225], v160 offset:56320
	global_load_lds_dwordx4 v[226:227], off
	s_add_i32 m0, s2, 0x2000
	s_add_u32 s2, s40, 0x80080
	v_lshl_add_u64 v[226:227], v[228:229], 0, s[20:21]
	s_addc_u32 s3, s41, 0
	s_add_i32 s10, s11, s48
	global_load_lds_dwordx4 v[226:227], off
	v_lshl_add_u64 v[226:227], s[2:3], 0, v[132:133]
	s_mov_b32 m0, s10
	s_nop 0
	global_load_lds_dwordx4 v[226:227], off
	v_lshl_add_u64 v[226:227], s[2:3], 0, v[134:135]
	s_add_i32 m0, s10, 0x2000
	s_nop 0
	global_load_lds_dwordx4 v[226:227], off
	v_lshl_add_u64 v[226:227], v[230:231], 0, s[20:21]
	s_mov_b32 m0, s58
	s_nop 0
	global_load_lds_dwordx4 v[226:227], off
	v_lshl_add_u64 v[226:227], v[232:233], 0, s[20:21]
	s_mov_b32 m0, s59
	s_nop 0
	global_load_lds_dwordx4 v[226:227], off
	s_waitcnt vmcnt(8)
	s_waitcnt lgkmcnt(0)
	s_barrier
	s_waitcnt lgkmcnt(0)
	v_mfma_f32_16x16x32_bf16 v[62:65], v[152:155], v[194:197], v[62:65]
	v_mfma_f32_16x16x32_bf16 v[58:61], v[170:173], v[194:197], v[58:61]
	v_mfma_f32_16x16x32_bf16 v[46:49], v[152:155], v[202:205], v[46:49]
	v_mfma_f32_16x16x32_bf16 v[42:45], v[170:173], v[202:205], v[42:45]
	v_mfma_f32_16x16x32_bf16 v[30:33], v[152:155], v[210:213], v[30:33]
	v_mfma_f32_16x16x32_bf16 v[26:29], v[170:173], v[210:213], v[26:29]
	v_mfma_f32_16x16x32_bf16 v[14:17], v[152:155], v[218:221], v[14:17]
	v_mfma_f32_16x16x32_bf16 v[10:13], v[170:173], v[218:221], v[10:13]
	v_mfma_f32_16x16x32_bf16 v[62:65], v[166:169], v[198:201], v[62:65]
	v_mfma_f32_16x16x32_bf16 v[58:61], v[174:177], v[198:201], v[58:61]
	v_mfma_f32_16x16x32_bf16 v[46:49], v[166:169], v[206:209], v[46:49]
	v_mfma_f32_16x16x32_bf16 v[42:45], v[174:177], v[206:209], v[42:45]
	v_mfma_f32_16x16x32_bf16 v[30:33], v[166:169], v[214:217], v[30:33]
	v_mfma_f32_16x16x32_bf16 v[26:29], v[174:177], v[214:217], v[26:29]
	v_mfma_f32_16x16x32_bf16 v[14:17], v[166:169], v[222:225], v[14:17]
	v_mfma_f32_16x16x32_bf16 v[10:13], v[174:177], v[222:225], v[10:13]
	v_mfma_f32_16x16x32_bf16 v[54:57], v[178:181], v[194:197], v[54:57]
	v_mfma_f32_16x16x32_bf16 v[50:53], v[186:189], v[194:197], v[50:53]
	v_mfma_f32_16x16x32_bf16 v[38:41], v[178:181], v[202:205], v[38:41]
	v_mfma_f32_16x16x32_bf16 v[34:37], v[186:189], v[202:205], v[34:37]
	v_mfma_f32_16x16x32_bf16 v[22:25], v[178:181], v[210:213], v[22:25]
	v_mfma_f32_16x16x32_bf16 v[18:21], v[186:189], v[210:213], v[18:21]
	v_mfma_f32_16x16x32_bf16 v[6:9], v[178:181], v[218:221], v[6:9]
	v_mfma_f32_16x16x32_bf16 v[2:5], v[186:189], v[218:221], v[2:5]
	v_mfma_f32_16x16x32_bf16 v[54:57], v[182:185], v[198:201], v[54:57]
	v_mfma_f32_16x16x32_bf16 v[50:53], v[190:193], v[198:201], v[50:53]
	v_mfma_f32_16x16x32_bf16 v[38:41], v[182:185], v[206:209], v[38:41]
	v_mfma_f32_16x16x32_bf16 v[34:37], v[190:193], v[206:209], v[34:37]
	v_mfma_f32_16x16x32_bf16 v[22:25], v[182:185], v[214:217], v[22:25]
	v_mfma_f32_16x16x32_bf16 v[18:21], v[190:193], v[214:217], v[18:21]
	v_mfma_f32_16x16x32_bf16 v[6:9], v[182:185], v[222:225], v[6:9]
	v_mfma_f32_16x16x32_bf16 v[2:5], v[190:193], v[222:225], v[2:5]
	s_barrier
	s_add_i32 s66, s66, 2
	s_cmp_gt_u32 s66, 29
	s_mov_b64 s[10:11], s[38:39]
	s_cbranch_scc0 .LBB0_1005
	s_and_b64 vcc, exec, s[24:25]
	s_cbranch_vccz .LBB0_1008
	s_barrier
